# attention fast-path prologue: first three K tiles and two V tiles loaded in one round trip instead of serial waits
# baseline (speedup 1.0000x reference)
.LBB0_1614:
	s_and_b64 vcc, exec, s[2:3]
	s_cbranch_vccz .LBB0_1570
	v_mov_b32_e32 v150, v0
	s_nop 0
	v_ashrrev_i32_e32 v4, 4, v150
	v_and_b32_e32 v8, 15, v150
	v_ashrrev_i32_e32 v5, 31, v4
	v_cmp_gt_u32_e32 vcc, 8, v8
	v_lshl_add_u64 v[6:7], s[42:43], 0, v[4:5]
	v_lshlrev_b32_e32 v2, 4, v8
	s_and_saveexec_b64 s[2:3], vcc
	s_xor_b64 s[2:3], exec, s[2:3]
	v_lshlrev_b64 v[6:7], 11, v[6:7]
	v_lshl_add_u64 v[6:7], s[8:9], 0, v[6:7]
	s_lshl_b32 s20, s52, 8
	s_mov_b32 s21, s35
	v_lshl_add_u64 v[6:7], v[6:7], 0, s[20:21]
	s_lshl_b32 s34, s52, 7
	v_lshl_add_u64 v[138:139], v[6:7], 0, v[2:3]
	s_or_saveexec_b64 s[2:3], s[2:3]
	v_mov_b64_e32 v[26:27], 0x400
	v_mov_b64_e32 v[24:25], s[34:35]
	s_xor_b64 exec, exec, s[2:3]
	v_lshlrev_b64 v[6:7], 6, v[6:7]
	v_lshl_add_u64 v[6:7], s[10:11], 0, v[6:7]
	s_movk_i32 s20, 0xff80
	v_lshl_add_u64 v[6:7], v[6:7], 0, v[2:3]
	s_mov_b32 s21, -1
	s_lshl_b32 s34, s52, 7
	v_lshl_add_u64 v[138:139], v[6:7], 0, s[20:21]
	v_mov_b64_e32 v[26:27], 32
	v_mov_b64_e32 v[24:25], s[34:35]
	s_or_b64 exec, exec, s[2:3]
	v_cmp_lt_u32_e64 s[2:3], 11, v8
	v_cmp_gt_u32_e64 s[38:39], 12, v8
	v_lshlrev_b32_e32 v30, 6, v26
	s_and_saveexec_b64 s[26:27], s[38:39]
	s_cbranch_execz .LBB0_1621
	v_mov_b32_e32 v31, v3
	v_lshl_add_u64 v[6:7], v[138:139], 0, v[30:31]
	global_load_dwordx4 v[108:111], v[138:139], off
	global_load_dwordx4 v[112:115], v[6:7], off
	v_lshlrev_b32_e32 v40, 7, v26
	v_mov_b32_e32 v41, v3
	v_lshl_add_u64 v[40:41], v[138:139], 0, v[40:41]
	v_lshl_add_u64 v[42:43], v[40:41], 0, v[30:31]
	global_load_dwordx4 v[120:123], v[40:41], off
	global_load_dwordx4 v[124:127], v[42:43], off
	v_lshlrev_b32_e32 v44, 8, v26
	v_mov_b32_e32 v45, v3
	v_lshl_add_u64 v[44:45], v[138:139], 0, v[44:45]
	v_lshl_add_u64 v[46:47], v[44:45], 0, v[30:31]
	global_load_dwordx4 v[128:131], v[44:45], off
	global_load_dwordx4 v[132:135], v[46:47], off
.LBB0_1621:
	s_or_b64 exec, exec, s[26:27]
	v_ashrrev_i32_e32 v28, 3, v150
	v_ashrrev_i32_e32 v29, 31, v28
	v_lshl_add_u64 v[6:7], s[42:43], 0, v[28:29]
	v_lshlrev_b32_e32 v5, 3, v150
	v_lshlrev_b64 v[6:7], 11, v[6:7]
	v_and_b32_e32 v10, 56, v5
	v_lshl_add_u64 v[6:7], s[8:9], 0, v[6:7]
	v_lshl_add_u64 v[6:7], v[24:25], 1, v[6:7]
	v_lshlrev_b32_e32 v136, 1, v10
	v_mov_b32_e32 v137, v3
	v_lshl_add_u64 v[8:9], v[6:7], 0, v[136:137]
	v_lshlrev_b32_e32 v27, 8, v4
	v_and_b32_e32 v4, 0xf0, v150
	v_bitop3_b32 v154, v2, v27, v4 bitop3:0xde
	global_load_dwordx4 v[4:7], v[8:9], off offset:128
	v_lshl_add_u64 v[40:41], v[8:9], 0, s[24:25]
	v_add_co_u32_e32 v40, vcc, 0x20000, v40
	s_nop 0
	v_addc_co_u32_e32 v41, vcc, 0, v41, vcc
	global_load_dwordx4 v[20:23], v[40:41], off
	v_add_co_u32_e32 v40, vcc, 0x20000, v40
	s_nop 0
	v_addc_co_u32_e32 v41, vcc, 0, v41, vcc
	global_load_dwordx4 v[116:119], v[40:41], off
	s_movk_i32 s19, 0xf0
	s_waitcnt vmcnt(0)
	v_bitop3_b32 v34, v2, v150, s19 bitop3:0x78
	v_add_u32_e32 v35, 0, v154
	v_add3_u32 v11, v27, v34, 0
	s_and_saveexec_b64 s[26:27], s[38:39]
	s_cbranch_execz .LBB0_1623
	v_lshlrev_b32_e32 v2, 7, v26
	s_waitcnt vmcnt(2)
	ds_write_b128 v35, v[108:111]
	s_waitcnt vmcnt(1)
	ds_write_b128 v11, v[112:115] offset:8192
	ds_write_b128 v35, v[120:123] offset:16384
	ds_write_b128 v11, v[124:127] offset:24576
	ds_write_b128 v35, v[128:131] offset:32768
	ds_write_b128 v11, v[132:135] offset:40960
	s_movk_i32 s20, 0x180
	v_mad_u64_u32 v[40:41], vcc, v26, s20, v[138:139]
	v_mov_b32_e32 v31, v3
	v_lshl_add_u64 v[42:43], v[40:41], 0, v[30:31]
	global_load_dwordx4 v[108:111], v[40:41], off
	global_load_dwordx4 v[112:115], v[42:43], off
	v_mov_b32_e32 v31, v3
.LBB0_1623:
	s_or_b64 exec, exec, s[26:27]
	v_and_b32_e32 v2, 0x1fffff0, v28
	v_lshlrev_b32_e32 v12, 1, v28
	v_and_or_b32 v2, v12, 8, v2
	v_lshrrev_b32_e32 v2, 2, v2
	v_lshrrev_b32_e32 v10, 5, v10
	v_lshrrev_b32_e32 v12, 1, v28
	v_or_b32_e32 v2, v2, v10
	v_and_b32_e32 v10, 3, v28
	v_and_or_b32 v10, v12, 4, v10
	v_lshlrev_b32_e32 v2, 9, v2
	v_lshlrev_b32_e32 v10, 6, v10
	v_and_b32_e32 v12, 48, v136
	v_or3_b32 v2, v12, v10, v2
	v_add_u32_e32 v156, 0, v2
	ds_write_b128 v156, v[4:7] offset:49152
	ds_write_b128 v156, v[20:23] offset:57344
	v_lshlrev_b32_e32 v2, 8, v26
	s_and_saveexec_b64 s[26:27], s[38:39]
	s_cbranch_execz .LBB0_1625
	v_mov_b32_e32 v31, v3
.LBB0_1625:
	s_or_b64 exec, exec, s[26:27]
	v_lshl_add_u64 v[32:33], v[8:9], 0, s[24:25]
	v_and_b32_e32 v137, 31, v150
	v_bfe_u32 v151, v150, 5, 1
	v_lshlrev_b32_e32 v153, 4, v151
	v_lshlrev_b32_e32 v162, 8, v137
	v_lshlrev_b32_e32 v31, 4, v150
	v_add_u32_e32 v164, 0, v162
	v_bitop3_b32 v165, v153, v31, s19 bitop3:0x78
	s_waitcnt lgkmcnt(0)
	s_barrier
	v_add_u32_e32 v158, v164, v165
	ds_read_b128 v[4:7], v158
	ds_read_b128 v[36:39], v158 offset:8192
	v_and_b32_e32 v31, 0xf0, v31
	v_bitop3_b32 v166, v153, v31, 32 bitop3:0x36
	v_add_u32_e32 v163, v164, v166
	ds_read_b128 v[52:55], v163
	s_waitcnt lgkmcnt(2)
	v_mfma_f32_32x32x16_bf16 v[4:19], v[4:7], v[100:103], 0
	v_bitop3_b32 v167, v153, v31, 64 bitop3:0x36
	v_add_u32_e32 v159, v164, v167
	s_movk_i32 s19, 0x60
	v_bitop3_b32 v168, v153, v31, s19 bitop3:0x36
	v_add_u32_e32 v160, v164, v168
	s_movk_i32 s19, 0x80
	v_bitop3_b32 v169, v153, v31, s19 bitop3:0x36
	s_waitcnt lgkmcnt(0)
	v_mfma_f32_32x32x16_bf16 v[4:19], v[52:55], v[96:99], v[4:19]
	ds_read_b128 v[52:55], v163 offset:8192
	v_add_u32_e32 v161, v164, v169
	s_movk_i32 s19, 0xa0
	v_bitop3_b32 v170, v153, v31, s19 bitop3:0x36
	v_add_u32_e32 v157, v164, v170
	v_add_u32_e32 v171, v27, v34
	v_mfma_f32_32x32x16_bf16 v[36:51], v[36:39], v[100:103], 0
	s_waitcnt lgkmcnt(0)
	v_mfma_f32_32x32x16_bf16 v[36:51], v[52:55], v[96:99], v[36:51]
	ds_read_b128 v[52:55], v159
	s_waitcnt lgkmcnt(0)
	v_mfma_f32_32x32x16_bf16 v[4:19], v[52:55], v[104:107], v[4:19]
	ds_read_b128 v[52:55], v159 offset:8192
	s_waitcnt lgkmcnt(0)
	v_mfma_f32_32x32x16_bf16 v[36:51], v[52:55], v[104:107], v[36:51]
	ds_read_b128 v[52:55], v160
	s_waitcnt lgkmcnt(0)
	v_mfma_f32_32x32x16_bf16 v[4:19], v[52:55], v[92:95], v[4:19]
	ds_read_b128 v[52:55], v160 offset:8192
	s_waitcnt lgkmcnt(0)
	v_mfma_f32_32x32x16_bf16 v[36:51], v[52:55], v[92:95], v[36:51]
	ds_read_b128 v[52:55], v161
	s_waitcnt lgkmcnt(0)
	v_mfma_f32_32x32x16_bf16 v[4:19], v[52:55], v[88:91], v[4:19]
	ds_read_b128 v[52:55], v161 offset:8192
	s_waitcnt lgkmcnt(0)
	v_mfma_f32_32x32x16_bf16 v[36:51], v[52:55], v[88:91], v[36:51]
	ds_read_b128 v[52:55], v157
	s_waitcnt lgkmcnt(0)
	v_mfma_f32_32x32x16_bf16 v[4:19], v[52:55], v[84:87], v[4:19]
	ds_read_b128 v[52:55], v157 offset:8192
	s_waitcnt lgkmcnt(0)
	v_mfma_f32_32x32x16_bf16 v[36:51], v[52:55], v[84:87], v[36:51]
	s_and_saveexec_b64 s[20:21], s[2:3]
	s_xor_b64 s[2:3], exec, s[20:21]
	v_add_u32_e32 v171, v27, v34
	s_andn2_saveexec_b64 s[2:3], s[2:3]
	s_cbranch_execz .LBB0_1629
	v_add_u32_e32 v27, 0, v171
	s_movk_i32 s19, 0x180
	v_mov_b32_e32 v31, v3
.LBB0_1629:
	s_or_b64 exec, exec, s[2:3]
	s_mov_b32 s2, 0x40000
	s_nop 1
	v_exp_f32_e32 v174, v4
	v_exp_f32_e32 v176, v5
	s_nop 0
	v_and_b32_e32 v152, 63, v150
	v_lshlrev_b32_e32 v5, 4, v152
	v_exp_f32_e32 v178, v6
	v_lshlrev_b32_e32 v4, 3, v152
	v_and_b32_e32 v5, 0xc0, v5
	v_lshlrev_b32_e32 v6, 1, v152
	v_and_or_b32 v5, v4, 24, v5
	v_and_b32_e32 v6, 32, v6
	v_and_b32_e32 v4, 0x100, v4
	v_or3_b32 v155, v5, v6, v4
	v_bitop3_b32 v4, v151, v150, 15 bitop3:0x78
	s_waitcnt lgkmcnt(0)
	s_barrier
	v_and_b32_e32 v6, 15, v150
	v_lshl_add_u32 v4, v4, 4, v164
	ds_read_b128 v[52:55], v4 offset:16384
	ds_read_b128 v[56:59], v4 offset:24576
	v_bitop3_b32 v4, v151, v6, 2 bitop3:0x36
	v_lshl_add_u32 v4, v4, 4, v164
	ds_read_b128 v[132:135], v4 offset:16384
	ds_read_b128 v[124:127], v4 offset:24576
	v_bitop3_b32 v4, v151, v6, 4 bitop3:0x36
	v_and_b32_e32 v6, 7, v6
	v_lshl_add_u32 v4, v4, 4, v164
	ds_read_b128 v[128:131], v4 offset:16384
	ds_read_b128 v[120:123], v4 offset:24576
	s_lshl_b64 s[20:21], s[36:37], 23
	v_lshlrev_b64 v[4:5], 11, v[28:29]
	v_exp_f32_e32 v180, v7
	v_exp_f32_e32 v182, v8
	v_exp_f32_e32 v184, v9
	v_exp_f32_e32 v186, v10
	v_exp_f32_e32 v187, v11
	v_exp_f32_e32 v175, v12
	v_exp_f32_e32 v177, v13
	v_exp_f32_e32 v179, v14
	v_exp_f32_e32 v181, v15
	v_exp_f32_e32 v183, v16
	v_exp_f32_e32 v185, v17
	v_exp_f32_e32 v188, v18
	v_exp_f32_e32 v189, v19
	v_lshl_add_u64 v[4:5], s[20:21], 0, v[4:5]
	v_lshl_or_b32 v4, v6, 4, v4
	v_lshl_add_u64 v[4:5], v[24:25], 1, v[4:5]
	v_mov_b32_e32 v173, 0
	s_mov_b32 s2, 1
	s_mov_b32 s34, 0
	s_mov_b32 s40, 2
	v_add_u32_e32 v172, 0, v155
	v_mul_hi_u32_u24_e32 v141, 0x2c0, v26
	v_mul_u32_u24_e32 v140, 0x2c0, v26
	v_mul_hi_u32_u24_e32 v143, 0x280, v26
	v_mul_u32_u24_e32 v142, 0x280, v26
	v_mul_hi_u32_u24_e32 v145, 0x240, v26
	v_mul_u32_u24_e32 v144, 0x240, v26
	v_lshlrev_b32_e32 v146, 9, v26
	v_mov_b32_e32 v147, v3
	v_lshl_add_u64 v[148:149], s[14:15], 0, v[4:5]
	s_mov_b32 s3, 0
	s_mov_b32 s41, 1
	s_mov_b32 s43, 2
	s_mov_b32 s42, 1
	v_mov_b32_e32 v4, 0
	v_mov_b32_e32 v5, v173
	v_mov_b32_e32 v6, v173
	v_mov_b32_e32 v7, v173
	v_mov_b32_e32 v8, v173
	v_mov_b32_e32 v9, v173
	v_mov_b32_e32 v10, v173
	v_mov_b32_e32 v11, v173
	v_mov_b32_e32 v12, v173
	v_mov_b32_e32 v13, v173
	v_mov_b32_e32 v14, v173
	v_mov_b32_e32 v15, v173
	v_mov_b32_e32 v16, v173
	v_mov_b32_e32 v17, v173
	v_mov_b32_e32 v18, v173
	v_mov_b32_e32 v19, v173
	v_mov_b32_e32 v20, 0
	v_mov_b32_e32 v21, v173
	v_mov_b32_e32 v22, v173
	v_mov_b32_e32 v23, v173
	v_mov_b32_e32 v24, v173
	v_mov_b32_e32 v25, v173
	v_mov_b32_e32 v26, v173
	v_mov_b32_e32 v27, v173
	v_mov_b32_e32 v28, v173
	v_mov_b32_e32 v29, v173
	v_mov_b32_e32 v30, v173
	v_mov_b32_e32 v31, v173
	v_mov_b32_e32 v32, v173
	v_mov_b32_e32 v33, v173
	v_mov_b32_e32 v34, v173
	v_mov_b32_e32 v35, v173
